# speedup vs baseline: 1.0064x; 1.0064x over previous
.LBB2_6:
	s_load_dwordx2 s[20:21], s[0:1], 0x0
	s_load_dwordx4 s[24:27], s[0:1], 0x10
	s_mov_b32 s16, s10
	s_mov_b32 s17, s9
	v_mov_b32_e32 v101, v130
	s_lshl_b32 s18, s16, 18
	s_lshl_b32 s19, s17, 17
	s_add_u32 s18, s18, s19
	v_lshl_or_b32 v100, s17, 13, v101
	v_lshlrev_b32_e32 v2, 2, v0
	s_lshl_b32 s28, s16, 9
	s_waitcnt lgkmcnt(0)
	s_add_u32 s20, s20, s18
	s_addc_u32 s21, s21, 0
	s_add_u32 s22, s20, 0x10000
	s_addc_u32 s23, s21, 0
	s_add_u32 s24, s24, s28
	s_addc_u32 s25, s25, 0
	s_add_u32 s26, s26, s28
	s_addc_u32 s27, s27, 0
	global_load_dwordx4 v[4:7], v101, s[20:21]
	global_load_dwordx4 v[8:11], v101, s[20:21] offset:1024
	global_load_dwordx4 v[12:15], v101, s[20:21] offset:2048
	global_load_dwordx4 v[16:19], v101, s[20:21] offset:3072
	global_load_dwordx4 v[20:23], v101, s[22:23]
	global_load_dwordx4 v[24:27], v101, s[22:23] offset:1024
	global_load_dwordx4 v[28:31], v101, s[22:23] offset:2048
	global_load_dwordx4 v[32:35], v101, s[22:23] offset:3072
	s_add_u32 s20, s20, 0x1000
	s_addc_u32 s21, s21, 0
	s_add_u32 s22, s22, 0x1000
	s_addc_u32 s23, s23, 0
	global_load_dwordx4 v[36:39], v101, s[20:21]
	global_load_dwordx4 v[40:43], v101, s[20:21] offset:1024
	global_load_dwordx4 v[44:47], v101, s[20:21] offset:2048
	global_load_dwordx4 v[48:51], v101, s[20:21] offset:3072
	global_load_dwordx4 v[52:55], v101, s[22:23]
	global_load_dwordx4 v[56:59], v101, s[22:23] offset:1024
	global_load_dwordx4 v[60:63], v101, s[22:23] offset:2048
	global_load_dwordx4 v[64:67], v101, s[22:23] offset:3072
	s_add_u32 s20, s20, 0x1000
	s_addc_u32 s21, s21, 0
	s_add_u32 s22, s22, 0x1000
	s_addc_u32 s23, s23, 0
	global_load_dwordx4 v[68:71], v101, s[20:21]
	global_load_dwordx4 v[72:75], v101, s[20:21] offset:1024
	global_load_dwordx4 v[76:79], v101, s[20:21] offset:2048
	global_load_dwordx4 v[80:83], v101, s[20:21] offset:3072
	global_load_dwordx4 v[84:87], v101, s[22:23]
	global_load_dwordx4 v[88:91], v101, s[22:23] offset:1024
	global_load_dwordx4 v[92:95], v101, s[22:23] offset:2048
	global_load_dwordx4 v[96:99], v101, s[22:23] offset:3072
	s_add_u32 s20, s20, 0x1000
	s_addc_u32 s21, s21, 0
	s_add_u32 s22, s22, 0x1000
	s_addc_u32 s23, s23, 0
	global_load_dword v1, v2, s[24:25] offset:-1024
	global_load_dword v3, v2, s[26:27] offset:-1024
	s_waitcnt vmcnt(25)
	ds_write_b128 v100, v[4:7]
	s_waitcnt vmcnt(24)
	ds_write_b128 v100, v[8:11] offset:1024
	s_waitcnt vmcnt(23)
	ds_write_b128 v100, v[12:15] offset:2048
	s_waitcnt vmcnt(22)
	ds_write_b128 v100, v[16:19] offset:3072
	s_waitcnt vmcnt(21)
	ds_write_b128 v100, v[20:23] offset:4096
	s_waitcnt vmcnt(20)
	ds_write_b128 v100, v[24:27] offset:5120
	s_waitcnt vmcnt(19)
	ds_write_b128 v100, v[28:31] offset:6144
	s_waitcnt vmcnt(18)
	ds_write_b128 v100, v[32:35] offset:7168
	s_waitcnt lgkmcnt(0)
	s_barrier
	global_load_dwordx4 v[4:7], v101, s[20:21]
	global_load_dwordx4 v[8:11], v101, s[20:21] offset:1024
	global_load_dwordx4 v[12:15], v101, s[20:21] offset:2048
	global_load_dwordx4 v[16:19], v101, s[20:21] offset:3072
	global_load_dwordx4 v[20:23], v101, s[22:23]
	global_load_dwordx4 v[24:27], v101, s[22:23] offset:1024
	global_load_dwordx4 v[28:31], v101, s[22:23] offset:2048
	global_load_dwordx4 v[32:35], v101, s[22:23] offset:3072
	s_add_u32 s20, s20, 0x1000
	s_addc_u32 s21, s21, 0
	s_add_u32 s22, s22, 0x1000
	s_addc_u32 s23, s23, 0
	s_waitcnt vmcnt(25)
	ds_write_b128 v100, v[36:39] offset:16384
	s_waitcnt vmcnt(24)
	ds_write_b128 v100, v[40:43] offset:17408
	s_waitcnt vmcnt(23)
	ds_write_b128 v100, v[44:47] offset:18432
	s_waitcnt vmcnt(22)
	ds_write_b128 v100, v[48:51] offset:19456
	s_waitcnt vmcnt(21)
	ds_write_b128 v100, v[52:55] offset:20480
	s_waitcnt vmcnt(20)
	ds_write_b128 v100, v[56:59] offset:21504
	s_waitcnt vmcnt(19)
	ds_write_b128 v100, v[60:63] offset:22528
	s_waitcnt vmcnt(18)
	ds_write_b128 v100, v[64:67] offset:23552
	s_waitcnt lgkmcnt(0)
	s_barrier
	global_load_dwordx4 v[36:39], v101, s[20:21]
	global_load_dwordx4 v[40:43], v101, s[20:21] offset:1024
	global_load_dwordx4 v[44:47], v101, s[20:21] offset:2048
	global_load_dwordx4 v[48:51], v101, s[20:21] offset:3072
	global_load_dwordx4 v[52:55], v101, s[22:23]
	global_load_dwordx4 v[56:59], v101, s[22:23] offset:1024
	global_load_dwordx4 v[60:63], v101, s[22:23] offset:2048
	global_load_dwordx4 v[64:67], v101, s[22:23] offset:3072
	s_add_u32 s20, s20, 0x1000
	s_addc_u32 s21, s21, 0
	s_add_u32 s22, s22, 0x1000
	s_addc_u32 s23, s23, 0
	s_waitcnt vmcnt(25)
	ds_write_b128 v100, v[68:71]
	s_waitcnt vmcnt(24)
	ds_write_b128 v100, v[72:75] offset:1024
	s_waitcnt vmcnt(23)
	ds_write_b128 v100, v[76:79] offset:2048
	s_waitcnt vmcnt(22)
	ds_write_b128 v100, v[80:83] offset:3072
	s_waitcnt vmcnt(21)
	ds_write_b128 v100, v[84:87] offset:4096
	s_waitcnt vmcnt(20)
	ds_write_b128 v100, v[88:91] offset:5120
	s_waitcnt vmcnt(19)
	ds_write_b128 v100, v[92:95] offset:6144
	s_waitcnt vmcnt(18)
	ds_write_b128 v100, v[96:99] offset:7168
	s_waitcnt lgkmcnt(0)
	s_barrier
	global_load_dwordx4 v[68:71], v101, s[20:21]
	global_load_dwordx4 v[72:75], v101, s[20:21] offset:1024
	global_load_dwordx4 v[76:79], v101, s[20:21] offset:2048
	global_load_dwordx4 v[80:83], v101, s[20:21] offset:3072
	global_load_dwordx4 v[84:87], v101, s[22:23]
	global_load_dwordx4 v[88:91], v101, s[22:23] offset:1024
	global_load_dwordx4 v[92:95], v101, s[22:23] offset:2048
	global_load_dwordx4 v[96:99], v101, s[22:23] offset:3072
	s_add_u32 s20, s20, 0x1000
	s_addc_u32 s21, s21, 0
	s_add_u32 s22, s22, 0x1000
	s_addc_u32 s23, s23, 0
	s_waitcnt vmcnt(23)
	ds_write_b128 v100, v[4:7] offset:16384
	v_mul_f32_e32 v1, 0x4038aa3b, v1
	ds_write2st64_b32 v2, v1, v3 offset0:124 offset1:126
	s_waitcnt vmcnt(22)
	ds_write_b128 v100, v[8:11] offset:17408
	s_waitcnt vmcnt(21)
	ds_write_b128 v100, v[12:15] offset:18432
	s_waitcnt vmcnt(20)
	ds_write_b128 v100, v[16:19] offset:19456
	s_waitcnt vmcnt(19)
	ds_write_b128 v100, v[20:23] offset:20480
	s_waitcnt vmcnt(18)
	ds_write_b128 v100, v[24:27] offset:21504
	s_waitcnt vmcnt(17)
	ds_write_b128 v100, v[28:31] offset:22528
	s_waitcnt vmcnt(16)
	ds_write_b128 v100, v[32:35] offset:23552
	s_waitcnt lgkmcnt(0)
	s_barrier
	global_load_dwordx4 v[4:7], v101, s[20:21]
	global_load_dwordx4 v[8:11], v101, s[20:21] offset:1024
	global_load_dwordx4 v[12:15], v101, s[20:21] offset:2048
	global_load_dwordx4 v[16:19], v101, s[20:21] offset:3072
	global_load_dwordx4 v[20:23], v101, s[22:23]
	global_load_dwordx4 v[24:27], v101, s[22:23] offset:1024
	global_load_dwordx4 v[28:31], v101, s[22:23] offset:2048
	global_load_dwordx4 v[32:35], v101, s[22:23] offset:3072
	s_add_u32 s20, s20, 0x1000
	s_addc_u32 s21, s21, 0
	s_add_u32 s22, s22, 0x1000
	s_addc_u32 s23, s23, 0
	s_waitcnt vmcnt(23)
	ds_write_b128 v100, v[36:39]
	s_waitcnt vmcnt(22)
	ds_write_b128 v100, v[40:43] offset:1024
	s_waitcnt vmcnt(21)
	ds_write_b128 v100, v[44:47] offset:2048
	s_waitcnt vmcnt(20)
	ds_write_b128 v100, v[48:51] offset:3072
	s_waitcnt vmcnt(19)
	ds_write_b128 v100, v[52:55] offset:4096
	s_waitcnt vmcnt(18)
	ds_write_b128 v100, v[56:59] offset:5120
	s_waitcnt vmcnt(17)
	ds_write_b128 v100, v[60:63] offset:6144
	s_waitcnt vmcnt(16)
	ds_write_b128 v100, v[64:67] offset:7168
	s_waitcnt lgkmcnt(0)
	s_barrier
	global_load_dwordx4 v[36:39], v101, s[20:21]
	global_load_dwordx4 v[40:43], v101, s[20:21] offset:1024
	global_load_dwordx4 v[44:47], v101, s[20:21] offset:2048
	global_load_dwordx4 v[48:51], v101, s[20:21] offset:3072
	global_load_dwordx4 v[52:55], v101, s[22:23]
	global_load_dwordx4 v[56:59], v101, s[22:23] offset:1024
	global_load_dwordx4 v[60:63], v101, s[22:23] offset:2048
	global_load_dwordx4 v[64:67], v101, s[22:23] offset:3072
	s_add_u32 s20, s20, 0x1000
	s_addc_u32 s21, s21, 0
	s_add_u32 s22, s22, 0x1000
	s_addc_u32 s23, s23, 0
	s_waitcnt vmcnt(23)
	ds_write_b128 v100, v[68:71] offset:16384
	s_waitcnt vmcnt(22)
	ds_write_b128 v100, v[72:75] offset:17408
	s_waitcnt vmcnt(21)
	ds_write_b128 v100, v[76:79] offset:18432
	s_waitcnt vmcnt(20)
	ds_write_b128 v100, v[80:83] offset:19456
	s_waitcnt vmcnt(19)
	ds_write_b128 v100, v[84:87] offset:20480
	s_waitcnt vmcnt(18)
	ds_write_b128 v100, v[88:91] offset:21504
	s_waitcnt vmcnt(17)
	ds_write_b128 v100, v[92:95] offset:22528
	s_waitcnt vmcnt(16)
	ds_write_b128 v100, v[96:99] offset:23552
	s_waitcnt lgkmcnt(0)
	s_barrier
	global_load_dwordx4 v[68:71], v101, s[20:21]
	global_load_dwordx4 v[72:75], v101, s[20:21] offset:1024
	global_load_dwordx4 v[76:79], v101, s[20:21] offset:2048
	global_load_dwordx4 v[80:83], v101, s[20:21] offset:3072
	global_load_dwordx4 v[84:87], v101, s[22:23]
	global_load_dwordx4 v[88:91], v101, s[22:23] offset:1024
	global_load_dwordx4 v[92:95], v101, s[22:23] offset:2048
	global_load_dwordx4 v[96:99], v101, s[22:23] offset:3072
	s_add_u32 s20, s20, 0x1000
	s_addc_u32 s21, s21, 0
	s_add_u32 s22, s22, 0x1000
	s_addc_u32 s23, s23, 0
	s_waitcnt vmcnt(23)
	ds_write_b128 v100, v[4:7]
	s_waitcnt vmcnt(22)
	ds_write_b128 v100, v[8:11] offset:1024
	s_waitcnt vmcnt(21)
	ds_write_b128 v100, v[12:15] offset:2048
	s_waitcnt vmcnt(20)
	ds_write_b128 v100, v[16:19] offset:3072
	s_waitcnt vmcnt(19)
	ds_write_b128 v100, v[20:23] offset:4096
	s_waitcnt vmcnt(18)
	ds_write_b128 v100, v[24:27] offset:5120
	s_waitcnt vmcnt(17)
	ds_write_b128 v100, v[28:31] offset:6144
	s_waitcnt vmcnt(16)
	ds_write_b128 v100, v[32:35] offset:7168
	s_waitcnt lgkmcnt(0)
	s_barrier
	global_load_dwordx4 v[4:7], v101, s[20:21]
	global_load_dwordx4 v[8:11], v101, s[20:21] offset:1024
	global_load_dwordx4 v[12:15], v101, s[20:21] offset:2048
	global_load_dwordx4 v[16:19], v101, s[20:21] offset:3072
	global_load_dwordx4 v[20:23], v101, s[22:23]
	global_load_dwordx4 v[24:27], v101, s[22:23] offset:1024
	global_load_dwordx4 v[28:31], v101, s[22:23] offset:2048
	global_load_dwordx4 v[32:35], v101, s[22:23] offset:3072
	s_add_u32 s20, s20, 0x1000
	s_addc_u32 s21, s21, 0
	s_add_u32 s22, s22, 0x1000
	s_addc_u32 s23, s23, 0
	s_waitcnt vmcnt(23)
	ds_write_b128 v100, v[36:39] offset:16384
	s_waitcnt vmcnt(22)
	ds_write_b128 v100, v[40:43] offset:17408
	s_waitcnt vmcnt(21)
	ds_write_b128 v100, v[44:47] offset:18432
	s_waitcnt vmcnt(20)
	ds_write_b128 v100, v[48:51] offset:19456
	s_waitcnt vmcnt(19)
	ds_write_b128 v100, v[52:55] offset:20480
	s_waitcnt vmcnt(18)
	ds_write_b128 v100, v[56:59] offset:21504
	s_waitcnt vmcnt(17)
	ds_write_b128 v100, v[60:63] offset:22528
	s_waitcnt vmcnt(16)
	ds_write_b128 v100, v[64:67] offset:23552
	s_waitcnt lgkmcnt(0)
	s_barrier
	global_load_dwordx4 v[36:39], v101, s[20:21]
	global_load_dwordx4 v[40:43], v101, s[20:21] offset:1024
	global_load_dwordx4 v[44:47], v101, s[20:21] offset:2048
	global_load_dwordx4 v[48:51], v101, s[20:21] offset:3072
	global_load_dwordx4 v[52:55], v101, s[22:23]
	global_load_dwordx4 v[56:59], v101, s[22:23] offset:1024
	global_load_dwordx4 v[60:63], v101, s[22:23] offset:2048
	global_load_dwordx4 v[64:67], v101, s[22:23] offset:3072
	s_add_u32 s20, s20, 0x1000
	s_addc_u32 s21, s21, 0
	s_add_u32 s22, s22, 0x1000
	s_addc_u32 s23, s23, 0
	s_waitcnt vmcnt(23)
	ds_write_b128 v100, v[68:71]
	s_waitcnt vmcnt(22)
	ds_write_b128 v100, v[72:75] offset:1024
	s_waitcnt vmcnt(21)
	ds_write_b128 v100, v[76:79] offset:2048
	s_waitcnt vmcnt(20)
	ds_write_b128 v100, v[80:83] offset:3072
	s_waitcnt vmcnt(19)
	ds_write_b128 v100, v[84:87] offset:4096
	s_waitcnt vmcnt(18)
	ds_write_b128 v100, v[88:91] offset:5120
	s_waitcnt vmcnt(17)
	ds_write_b128 v100, v[92:95] offset:6144
	s_waitcnt vmcnt(16)
	ds_write_b128 v100, v[96:99] offset:7168
	s_waitcnt lgkmcnt(0)
	s_barrier
	global_load_dwordx4 v[68:71], v101, s[20:21]
	global_load_dwordx4 v[72:75], v101, s[20:21] offset:1024
	global_load_dwordx4 v[76:79], v101, s[20:21] offset:2048
	global_load_dwordx4 v[80:83], v101, s[20:21] offset:3072
	global_load_dwordx4 v[84:87], v101, s[22:23]
	global_load_dwordx4 v[88:91], v101, s[22:23] offset:1024
	global_load_dwordx4 v[92:95], v101, s[22:23] offset:2048
	global_load_dwordx4 v[96:99], v101, s[22:23] offset:3072
	s_add_u32 s20, s20, 0x1000
	s_addc_u32 s21, s21, 0
	s_add_u32 s22, s22, 0x1000
	s_addc_u32 s23, s23, 0
	s_waitcnt vmcnt(23)
	ds_write_b128 v100, v[4:7] offset:16384
	s_waitcnt vmcnt(22)
	ds_write_b128 v100, v[8:11] offset:17408
	s_waitcnt vmcnt(21)
	ds_write_b128 v100, v[12:15] offset:18432
	s_waitcnt vmcnt(20)
	ds_write_b128 v100, v[16:19] offset:19456
	s_waitcnt vmcnt(19)
	ds_write_b128 v100, v[20:23] offset:20480
	s_waitcnt vmcnt(18)
	ds_write_b128 v100, v[24:27] offset:21504
	s_waitcnt vmcnt(17)
	ds_write_b128 v100, v[28:31] offset:22528
	s_waitcnt vmcnt(16)
	ds_write_b128 v100, v[32:35] offset:23552
	s_waitcnt lgkmcnt(0)
	s_barrier
	global_load_dwordx4 v[4:7], v101, s[20:21]
	global_load_dwordx4 v[8:11], v101, s[20:21] offset:1024
	global_load_dwordx4 v[12:15], v101, s[20:21] offset:2048
	global_load_dwordx4 v[16:19], v101, s[20:21] offset:3072
	global_load_dwordx4 v[20:23], v101, s[22:23]
	global_load_dwordx4 v[24:27], v101, s[22:23] offset:1024
	global_load_dwordx4 v[28:31], v101, s[22:23] offset:2048
	global_load_dwordx4 v[32:35], v101, s[22:23] offset:3072
	s_add_u32 s20, s20, 0x1000
	s_addc_u32 s21, s21, 0
	s_add_u32 s22, s22, 0x1000
	s_addc_u32 s23, s23, 0
	s_waitcnt vmcnt(23)
	ds_write_b128 v100, v[36:39]
	s_waitcnt vmcnt(22)
	ds_write_b128 v100, v[40:43] offset:1024
	s_waitcnt vmcnt(21)
	ds_write_b128 v100, v[44:47] offset:2048
	s_waitcnt vmcnt(20)
	ds_write_b128 v100, v[48:51] offset:3072
	s_waitcnt vmcnt(19)
	ds_write_b128 v100, v[52:55] offset:4096
	s_waitcnt vmcnt(18)
	ds_write_b128 v100, v[56:59] offset:5120
	s_waitcnt vmcnt(17)
	ds_write_b128 v100, v[60:63] offset:6144
	s_waitcnt vmcnt(16)
	ds_write_b128 v100, v[64:67] offset:7168
	s_waitcnt lgkmcnt(0)
	s_barrier
	global_load_dwordx4 v[36:39], v101, s[20:21]
	global_load_dwordx4 v[40:43], v101, s[20:21] offset:1024
	global_load_dwordx4 v[44:47], v101, s[20:21] offset:2048
	global_load_dwordx4 v[48:51], v101, s[20:21] offset:3072
	global_load_dwordx4 v[52:55], v101, s[22:23]
	global_load_dwordx4 v[56:59], v101, s[22:23] offset:1024
	global_load_dwordx4 v[60:63], v101, s[22:23] offset:2048
	global_load_dwordx4 v[64:67], v101, s[22:23] offset:3072
	s_add_u32 s20, s20, 0x1000
	s_addc_u32 s21, s21, 0
	s_add_u32 s22, s22, 0x1000
	s_addc_u32 s23, s23, 0
	s_waitcnt vmcnt(23)
	ds_write_b128 v100, v[68:71] offset:16384
	s_waitcnt vmcnt(22)
	ds_write_b128 v100, v[72:75] offset:17408
	s_waitcnt vmcnt(21)
	ds_write_b128 v100, v[76:79] offset:18432
	s_waitcnt vmcnt(20)
	ds_write_b128 v100, v[80:83] offset:19456
	s_waitcnt vmcnt(19)
	ds_write_b128 v100, v[84:87] offset:20480
	s_waitcnt vmcnt(18)
	ds_write_b128 v100, v[88:91] offset:21504
	s_waitcnt vmcnt(17)
	ds_write_b128 v100, v[92:95] offset:22528
	s_waitcnt vmcnt(16)
	ds_write_b128 v100, v[96:99] offset:23552
	s_waitcnt lgkmcnt(0)
	s_barrier
	global_load_dwordx4 v[68:71], v101, s[20:21]
	global_load_dwordx4 v[72:75], v101, s[20:21] offset:1024
	global_load_dwordx4 v[76:79], v101, s[20:21] offset:2048
	global_load_dwordx4 v[80:83], v101, s[20:21] offset:3072
	global_load_dwordx4 v[84:87], v101, s[22:23]
	global_load_dwordx4 v[88:91], v101, s[22:23] offset:1024
	global_load_dwordx4 v[92:95], v101, s[22:23] offset:2048
	global_load_dwordx4 v[96:99], v101, s[22:23] offset:3072
	s_add_u32 s20, s20, 0x1000
	s_addc_u32 s21, s21, 0
	s_add_u32 s22, s22, 0x1000
	s_addc_u32 s23, s23, 0
	s_waitcnt vmcnt(23)
	ds_write_b128 v100, v[4:7]
	s_waitcnt vmcnt(22)
	ds_write_b128 v100, v[8:11] offset:1024
	s_waitcnt vmcnt(21)
	ds_write_b128 v100, v[12:15] offset:2048
	s_waitcnt vmcnt(20)
	ds_write_b128 v100, v[16:19] offset:3072
	s_waitcnt vmcnt(19)
	ds_write_b128 v100, v[20:23] offset:4096
	s_waitcnt vmcnt(18)
	ds_write_b128 v100, v[24:27] offset:5120
	s_waitcnt vmcnt(17)
	ds_write_b128 v100, v[28:31] offset:6144
	s_waitcnt vmcnt(16)
	ds_write_b128 v100, v[32:35] offset:7168
	s_waitcnt lgkmcnt(0)
	s_barrier
	global_load_dwordx4 v[4:7], v101, s[20:21]
	global_load_dwordx4 v[8:11], v101, s[20:21] offset:1024
	global_load_dwordx4 v[12:15], v101, s[20:21] offset:2048
	global_load_dwordx4 v[16:19], v101, s[20:21] offset:3072
	global_load_dwordx4 v[20:23], v101, s[22:23]
	global_load_dwordx4 v[24:27], v101, s[22:23] offset:1024
	global_load_dwordx4 v[28:31], v101, s[22:23] offset:2048
	global_load_dwordx4 v[32:35], v101, s[22:23] offset:3072
	s_add_u32 s20, s20, 0x1000
	s_addc_u32 s21, s21, 0
	s_add_u32 s22, s22, 0x1000
	s_addc_u32 s23, s23, 0
	s_waitcnt vmcnt(23)
	ds_write_b128 v100, v[36:39] offset:16384
	s_waitcnt vmcnt(22)
	ds_write_b128 v100, v[40:43] offset:17408
	s_waitcnt vmcnt(21)
	ds_write_b128 v100, v[44:47] offset:18432
	s_waitcnt vmcnt(20)
	ds_write_b128 v100, v[48:51] offset:19456
	s_waitcnt vmcnt(19)
	ds_write_b128 v100, v[52:55] offset:20480
	s_waitcnt vmcnt(18)
	ds_write_b128 v100, v[56:59] offset:21504
	s_waitcnt vmcnt(17)
	ds_write_b128 v100, v[60:63] offset:22528
	s_waitcnt vmcnt(16)
	ds_write_b128 v100, v[64:67] offset:23552
	s_waitcnt lgkmcnt(0)
	s_barrier
	s_waitcnt vmcnt(15)
	ds_write_b128 v100, v[68:71]
	s_waitcnt vmcnt(14)
	ds_write_b128 v100, v[72:75] offset:1024
	s_waitcnt vmcnt(13)
	ds_write_b128 v100, v[76:79] offset:2048
	s_waitcnt vmcnt(12)
	ds_write_b128 v100, v[80:83] offset:3072
	s_waitcnt vmcnt(11)
	ds_write_b128 v100, v[84:87] offset:4096
	s_waitcnt vmcnt(10)
	ds_write_b128 v100, v[88:91] offset:5120
	s_waitcnt vmcnt(9)
	ds_write_b128 v100, v[92:95] offset:6144
	s_waitcnt vmcnt(8)
	ds_write_b128 v100, v[96:99] offset:7168
	s_waitcnt lgkmcnt(0)
	s_barrier
	s_waitcnt vmcnt(7)
	ds_write_b128 v100, v[4:7] offset:16384
	s_waitcnt vmcnt(6)
	ds_write_b128 v100, v[8:11] offset:17408
	s_waitcnt vmcnt(5)
	ds_write_b128 v100, v[12:15] offset:18432
	s_waitcnt vmcnt(4)
	ds_write_b128 v100, v[16:19] offset:19456
	s_waitcnt vmcnt(3)
	ds_write_b128 v100, v[20:23] offset:20480
	s_waitcnt vmcnt(2)
	ds_write_b128 v100, v[24:27] offset:21504
	s_waitcnt vmcnt(1)
	ds_write_b128 v100, v[28:31] offset:22528
	s_waitcnt vmcnt(0)
	ds_write_b128 v100, v[32:35] offset:23552
	s_waitcnt lgkmcnt(0)
	s_barrier
	s_endpgm
	s_nop 0
	s_nop 0
	s_nop 0
	s_nop 0
	s_nop 0
	s_nop 0
	s_nop 0
	s_nop 0
	s_nop 0
	s_nop 0
	s_nop 0
	s_nop 0
	s_nop 0
	s_nop 0
	s_nop 0
	s_nop 0
	s_nop 0
	s_nop 0
	s_nop 0
	s_nop 0
	s_nop 0
	s_nop 0
	s_nop 0
	s_nop 0
	s_nop 0
	s_nop 0
	s_nop 0
	s_nop 0
	s_nop 0
	s_nop 0
	s_nop 0
	s_nop 0
	s_nop 0
	s_nop 0
	s_nop 0
	s_nop 0
	s_nop 0
	s_nop 0
	s_nop 0
	s_nop 0
	s_nop 0
	s_nop 0
	s_nop 0
	s_nop 0
	s_nop 0
	s_nop 0
	s_nop 0
	s_nop 0
	s_nop 0
	s_nop 0
	s_nop 0
	s_nop 0
	s_nop 0
	s_nop 0
	s_nop 0
	s_nop 0
	s_nop 0
	s_nop 0
	s_nop 0
	s_endpgm
